# v55 + SB unit header: no wait on the previous unit's stores before issuing loads; pre-loop wait vmcnt(2) (tile 4's pair may still fly)
# speedup vs baseline: 1.0176x; 1.0039x over previous
; #define GAS __attribute__((address_space(1)))
; #define LAS __attribute__((address_space(3)))
; #define GAS __attribute__((address_space(1)))
; #define SB_ISSUE(j) do { int kt_ = kt_hi - (j); kt_ = kt_ < 0 ? 0 : kt_; LAS unsigned char* sl_ = lds + ((j) % NS) * 16384 + wid * 1024; \
;         dma16(ksrc + (size_t)kt_ * 64 * 1536, sl_); dma16(vsrc + (size_t)kt_ * 64 * 1536, sl_ + 8192); } while (0)
; __device__ __forceinline__ void sb_unit(LAS unsigned char* lds, int tid, const bf16_t* QKV, bf16_t* OA, float* OSS, int b, int h, int qb) {
;     asm volatile("" : "+v"(tid));
;     const int lane = tid & 63, r32 = lane & 31, hi = lane >> 5, wid = __builtin_amdgcn_readfirstlane(tid >> 6);
;     const size_t rowb = (size_t)b * SEQ; const int q0 = qb * 256;
;     const bf16_t* Qw = QKV + (rowb + q0 + wid * 32) * 1536 + h * 64;
;     const bf16_t* Kh = QKV + rowb * 1536 + 512 + h * 64; const bf16_t* Vh = Kh + 512;
;     const int kt_hi = (q0 >> 6) + 3, NT = kt_hi + 1, jd = 3 - (wid >> 1);
;     const bf16_t* ksrc = Kh + (size_t)lane * 1536 + wid * 8;
;     const bf16_t* vsrc = Vh + (size_t)(16 * (wid & 3) + (lane >> 2)) * 1536 + (wid >> 2) * 32 + (lane & 3) * 8;
;     ...
;     bf16x8 qr[4];
; #pragma unroll
;     for (int d0 = 0; d0 < 4; ++d0) qr[d0] = *(const GAS bf16x8*)(Qw + (size_t)r32 * 1536 + d0 * 16 + hi * 8);
; #pragma unroll
;     for (int j = 0; j < PF; ++j) SB_ISSUE(j);
;     asm volatile("" : "+v"(qr[0]), "+v"(qr[1]), "+v"(qr[2]), "+v"(qr[3]));
;     f32x16 o0 = {}, o1 = {}; float carry = 1.f; bool mydone = false;
;     const int q = q0 + wid * 32 + r32;
;     volatile LAS unsigned* flags = (volatile LAS unsigned*)(lds + FLAG_OFF);
;     const int vpo = ((lane >> 4) & 1) * 32 + (lane & 3) * 8 + (4 * hi + ((lane & 15) >> 2)) * 64;
.LBB0_876:
	v_mov_b32_e32 v8, v188
	s_ashr_i32 s8, s79, 7
	s_and_b32 s2, s78, 15
	v_readfirstlane_b32 s13, v8
	s_and_b32 s12, s79, 15
	s_ashr_i32 s14, s13, 6
	s_ashr_i32 s9, s8, 31
	s_lshl_b32 s95, s2, 2
	s_lshl_b64 s[90:91], s[8:9], 12
	s_lshl_b32 s2, s12, 8
	s_lshl_b32 s3, s14, 5
	s_bfe_u32 s94, s79, 0x30004
	v_writelane_b32 v255, s2, 42
	s_or_b32 s2, s90, s2
	s_ashr_i32 s6, s3, 31
	s_add_u32 s2, s2, s3
	s_addc_u32 s6, s91, s6
	s_mulk_i32 s6, 0xc00
	s_mul_hi_u32 s7, s2, 0xc00
	s_add_i32 s7, s7, s6
	s_mulk_i32 s2, 0xc00
	v_readlane_b32 s10, v255, 40
	s_add_u32 s2, s10, s2
	v_readlane_b32 s11, v255, 41
	v_and_b32_e32 v115, 31, v8
	s_addc_u32 s7, s11, s7
	s_lshl_b32 s6, s94, 6
	s_lshl_b32 s9, s94, 7
	v_writelane_b32 v255, s6, 43
	s_add_u32 s6, s2, s9
	v_mul_u32_u24_e32 v0, 0x600, v115
	v_bfe_u32 v9, v8, 5, 1
	s_addc_u32 s7, s7, 0
	v_lshlrev_b32_e32 v0, 1, v0
	v_lshl_add_u64 v[2:3], s[6:7], 0, v[0:1]
	v_lshlrev_b32_e32 v0, 4, v9
	v_lshl_add_u64 v[2:3], v[2:3], 0, v[0:1]
	global_load_dwordx4 v[66:69], v[2:3], off offset:96
	global_load_dwordx4 v[70:73], v[2:3], off offset:64
	global_load_dwordx4 v[74:77], v[2:3], off offset:32
	global_load_dwordx4 v[78:81], v[2:3], off
	s_mul_i32 s7, s8, 0xc00000
	s_mul_hi_i32 s6, s8, 0xc00000
	s_add_u32 s7, s10, s7
	s_addc_u32 s8, s11, s6
	s_add_u32 s6, s7, s9
	s_waitcnt lgkmcnt(8)
	v_and_b32_e32 v120, 63, v8
	s_addc_u32 s7, s8, 0
	s_lshl_b32 s10, s14, 4
	v_bfe_u32 v2, v8, 2, 4
	v_mul_u32_u24_e32 v0, 0x600, v120
	v_and_or_b32 v2, s10, 48, v2
	s_lshl_b32 s82, s12, 2
	s_lshl_b32 s8, s14, 3
	v_mul_u32_u24_e32 v4, 0x600, v2
	s_ashr_i32 s10, s13, 3
	v_lshlrev_b32_e32 v2, 3, v8
	v_lshlrev_b32_e32 v0, 1, v0
	s_ashr_i32 s9, s8, 31
	s_andn2_b32 s10, s10, 31
	v_and_b32_e32 v10, 24, v2
	s_or_b32 s15, s82, 3
	v_lshl_add_u64 v[2:3], s[6:7], 0, v[0:1]
	v_lshlrev_b32_e32 v0, 1, v4
	s_ashr_i32 s11, s10, 31
	v_lshl_add_u64 v[116:117], s[8:9], 1, v[2:3]
	v_lshl_add_u64 v[4:5], s[6:7], 0, v[0:1]
	s_mul_i32 s88, s15, 0x30000
	v_lshl_add_u64 v[4:5], s[10:11], 1, v[4:5]
	v_lshlrev_b32_e32 v0, 1, v10
	s_lshl_b32 s6, s14, 10
	v_lshl_add_u64 v[6:7], v[116:117], 0, s[88:89]
	v_lshl_add_u64 v[118:119], v[4:5], 0, v[0:1]
	s_add_i32 s33, s6, 0
	v_lshl_add_u64 v[6:7], v[6:7], 0, s[28:29]
	s_mov_b32 s6, m0
	s_mov_b32 m0, s33
	s_nop 0
	global_load_lds_dwordx4 v[6:7], off
	s_mov_b32 m0, s6
	v_lshl_add_u64 v[6:7], v[118:119], 0, s[88:89]
	s_add_i32 s6, s33, 0x2000
	v_lshl_add_u64 v[6:7], v[6:7], 0, s[30:31]
	s_mov_b32 s7, m0
	s_mov_b32 m0, s6
	s_nop 0
	global_load_lds_dwordx4 v[6:7], off
	s_mov_b32 m0, s7
	s_mul_i32 s6, s12, 0xc0000
	v_lshl_add_u64 v[2:3], v[116:117], 0, s[28:29]
	s_add_i32 s7, s33, 0x4000
	s_add_i32 s88, s6, 0x60000
	v_lshl_add_u64 v[4:5], v[118:119], 0, s[30:31]
	v_lshl_add_u64 v[6:7], v[2:3], 0, s[88:89]
	s_mov_b32 s8, m0
	s_mov_b32 m0, s7
	s_nop 0
	global_load_lds_dwordx4 v[6:7], off
	s_mov_b32 m0, s8
	s_add_i32 s7, s33, 0x6000
	v_lshl_add_u64 v[6:7], v[4:5], 0, s[88:89]
	s_mov_b32 s8, m0
	s_mov_b32 m0, s7
	s_nop 0
	global_load_lds_dwordx4 v[6:7], off
	s_mov_b32 m0, s8
	s_add_i32 s7, s33, 0x8000
	s_or_b32 s88, s6, 0x30000
	v_lshl_add_u64 v[2:3], v[2:3], 0, s[88:89]
	s_mov_b32 s8, m0
	s_mov_b32 m0, s7
	s_nop 0
	global_load_lds_dwordx4 v[2:3], off
	s_mov_b32 m0, s8
	s_add_i32 s7, s33, 0xa000
	v_lshl_add_u64 v[2:3], v[4:5], 0, s[88:89]
	s_mov_b32 s8, m0
	s_mov_b32 m0, s7
	s_nop 0
	global_load_lds_dwordx4 v[2:3], off
	s_mov_b32 m0, s8
	s_mov_b32 s7, s89
	v_lshl_add_u64 v[2:3], v[116:117], 0, s[6:7]
	v_lshl_add_u64 v[2:3], v[2:3], 0, s[28:29]
	s_add_i32 s8, s33, 0xc000
	s_mov_b32 s9, m0
	s_mov_b32 m0, s8
	s_nop 0
	global_load_lds_dwordx4 v[2:3], off
	s_mov_b32 m0, s9
	v_lshl_add_u64 v[2:3], v[118:119], 0, s[6:7]
	v_lshl_add_u64 v[2:3], v[2:3], 0, s[30:31]
	s_add_i32 s6, s33, 0xe000
	s_mov_b32 s7, m0
	s_mov_b32 m0, s6
	s_nop 0
	global_load_lds_dwordx4 v[2:3], off
	s_mov_b32 m0, s7
	v_sub_u32_e64 v0, s82, 1 clamp
	s_mov_b32 s7, 0x30000
	v_mul_lo_u32 v0, v0, s7
	v_lshl_add_u64 v[2:3], v[116:117], 0, v[0:1]
	v_lshl_add_u64 v[2:3], v[2:3], 0, s[28:29]
	s_add_i32 s6, s33, 0x10000
	s_mov_b32 s7, m0
	s_mov_b32 m0, s6
	s_nop 0
	global_load_lds_dwordx4 v[2:3], off
	s_mov_b32 m0, s7
	v_lshl_add_u64 v[2:3], v[118:119], 0, v[0:1]
	v_lshl_add_u64 v[2:3], v[2:3], 0, s[30:31]
	s_add_i32 s6, s33, 0x12000
	s_mov_b32 s7, m0
	s_mov_b32 m0, s6
	s_nop 0
	global_load_lds_dwordx4 v[2:3], off
	s_mov_b32 m0, s7
	v_lshlrev_b32_e32 v2, 4, v8
	v_lshlrev_b32_e32 v0, 1, v8
	v_and_b32_e32 v2, 0xc0, v2
	v_and_b32_e32 v0, 32, v0
	v_lshl_or_b32 v2, v9, 8, v2
	s_ashr_i32 s6, s13, 7
	v_or3_b32 v121, v2, v0, v10
	s_lshl_b32 s7, s14, 2
	v_lshlrev_b32_e32 v0, 2, v9
	v_or_b32_e32 v2, s3, v115
	s_add_i32 s88, s7, 0
	v_sub_u32_e32 v0, v2, v0
	s_lshl_b32 s7, s6, 6
	v_mov_b32_e32 v14, v1
	v_mov_b32_e32 v15, v1
	v_lshlrev_b32_e32 v114, 3, v9
	v_lshlrev_b32_e32 v123, 10, v9
	v_subrev_u32_e32 v124, s7, v0
	v_mov_b32_e32 v0, v1
	v_mov_b32_e32 v2, v1
	v_mov_b32_e32 v3, v1
	v_mov_b32_e32 v4, v1
	v_mov_b32_e32 v5, v1
	v_mov_b32_e32 v6, v1
	v_mov_b32_e32 v7, v1
	v_mov_b32_e32 v8, v1
	v_mov_b32_e32 v9, v1
	v_mov_b32_e32 v10, v1
	v_mov_b32_e32 v11, v1
	v_mov_b32_e32 v12, v1
	v_mov_b32_e32 v13, v1
	v_mov_b64_e32 v[32:33], v[14:15]
	v_mov_b64_e32 v[30:31], v[12:13]
	v_mov_b64_e32 v[28:29], v[10:11]
	v_mov_b64_e32 v[26:27], v[8:9]
	v_mov_b64_e32 v[24:25], v[6:7]
	v_mov_b64_e32 v[22:23], v[4:5]
	v_mov_b64_e32 v[20:21], v[2:3]
	v_mov_b64_e32 v[18:19], v[0:1]
	v_mov_b64_e32 v[16:17], v[14:15]
	s_mov_b32 s2, 5
	s_add_i32 s83, s82, 4
	s_add_i32 s88, s88, 0x20200
	v_lshlrev_b32_e32 v122, 4, v115
	s_mov_b32 s81, 0
	v_cmp_eq_u32_e64 s[8:9], 0, v120
	s_add_i32 s76, s95, 4
	s_sub_i32 s97, 0, s6
	v_mov_b32_e32 v125, 1.0
	s_mov_b64 s[10:11], 0
	s_mov_b32 s80, -2
	s_mov_b32 s77, 0
	s_mov_b32 s6, 0
	v_mov_b64_e32 v[14:15], v[12:13]
	v_mov_b64_e32 v[12:13], v[10:11]
	v_mov_b64_e32 v[10:11], v[8:9]
	v_mov_b64_e32 v[8:9], v[6:7]
	v_mov_b64_e32 v[6:7], v[4:5]
	v_mov_b64_e32 v[4:5], v[2:3]
	v_mov_b64_e32 v[2:3], v[0:1]
	s_waitcnt vmcnt(2)
	s_branch .LBB0_878
